# speedup vs baseline: 1.0274x; 1.0073x over previous
_Z7gemm128ILi3ELi96EEv8GemmArgs:
	s_cmp_ge_u32 s2, 0x100
	s_cbranch_scc1 .Ldn_exit
	s_load_dwordx4 s[4:7], s[0:1], 0x0
	s_load_dwordx2 s[8:9], s[0:1], 0x20
	s_load_dwordx2 s[10:11], s[0:1], 0x38
	s_and_b32 s12, s2, 7
	s_lshr_b32 s13, s2, 3
	s_lshl_b32 s12, s12, 5
	s_add_u32 s12, s12, s13
	s_and_b32 s13, s12, 3
	s_lshr_b32 s12, s12, 2
	s_lshl_b32 s12, s12, 7
	s_mul_i32 s13, s13, 0xc0
	v_lshrrev_b32_e32 v1, 6, v0
	v_and_b32_e32 v14, 7, v0
	v_bfe_u32 v15, v0, 4, 3
	v_xor_b32_e32 v14, v14, v15
	v_readfirstlane_b32 s14, v1
	v_lshrrev_b32_e32 v15, 3, v0
	v_mul_u32_u24_e32 v15, 0x1800, v15
	v_lshl_add_u32 v2, v14, 4, v15
	s_mov_b32 s22, 0x30000
	v_add_u32_e32 v3, s22, v2
	v_add_u32_e32 v4, s22, v3
	v_add_u32_e32 v5, s22, v4
	v_add_u32_e32 v6, s22, v5
	v_add_u32_e32 v7, s22, v6
	v_and_b32_e32 v14, 15, v0
	v_bfe_u32 v15, v0, 4, 2
	v_lshrrev_b32_e32 v16, 1, v14
	v_xor_b32_e32 v16, v16, v15
	v_lshlrev_b32_e32 v16, 4, v16
	v_bfe_u32 v17, v0, 7, 1
	v_bfe_u32 v18, v0, 6, 1
	v_lshl_add_u32 v19, v17, 6, v14
	v_lshl_add_u32 v8, v19, 7, v16
	v_mul_u32_u24_e32 v19, 0x60, v18
	v_add_u32_e32 v19, v19, v14
	v_lshl_add_u32 v9, v19, 7, v16
	v_add_u32_e32 v9, 0x4000, v9
	v_lshl_add_u32 v19, v17, 6, v14
	v_add_u32_e32 v19, s12, v19
	v_mul_u32_u24_e32 v19, 0xc00, v19
	v_mul_u32_u24_e32 v60, 0x60, v18
	v_lshl_add_u32 v60, v15, 2, v60
	v_add_u32_e32 v60, s13, v60
	v_lshl_add_u32 v56, v60, 2, v19
	s_mov_b32 s22, 0xc000
	v_add_u32_e32 v57, s22, v56
	v_add_u32_e32 v58, s22, v57
	v_add_u32_e32 v59, s22, v58
	s_waitcnt lgkmcnt(0)
	s_mul_i32 s22, s12, 0x1800
	s_add_u32 s16, s4, s22
	s_addc_u32 s17, s5, 0
	s_mul_i32 s22, s13, 0x1800
	s_add_u32 s18, s6, s22
	s_addc_u32 s19, s7, 0
	s_lshl_b32 s20, s14, 10
	s_mov_b32 s21, 0
	s_add_u32 m0, s20, 0x0
	s_nop 0
	global_load_lds_dwordx4 v2, s[16:17]
	s_add_u32 m0, s20, 0x1000
	s_nop 0
	global_load_lds_dwordx4 v3, s[16:17]
	s_add_u32 m0, s20, 0x2000
	s_nop 0
	global_load_lds_dwordx4 v4, s[16:17]
	s_add_u32 m0, s20, 0x3000
	s_nop 0
	global_load_lds_dwordx4 v5, s[16:17]
	s_add_u32 m0, s20, 0x4000
	s_nop 0
	global_load_lds_dwordx4 v2, s[18:19]
	s_add_u32 m0, s20, 0x5000
	s_nop 0
	global_load_lds_dwordx4 v3, s[18:19]
	s_add_u32 m0, s20, 0x6000
	s_nop 0
	global_load_lds_dwordx4 v4, s[18:19]
	s_add_u32 m0, s20, 0x7000
	s_nop 0
	global_load_lds_dwordx4 v5, s[18:19]
	s_add_u32 m0, s20, 0x8000
	s_nop 0
	global_load_lds_dwordx4 v6, s[18:19]
	s_add_u32 m0, s20, 0x9000
	s_nop 0
	global_load_lds_dwordx4 v7, s[18:19]
	s_add_u32 s16, s16, 0x80
	s_addc_u32 s17, s17, 0
	s_add_u32 s18, s18, 0x80
	s_addc_u32 s19, s19, 0
	s_add_u32 s20, s20, 0xa000
	s_cmp_ge_u32 s20, 0x28000
	s_cbranch_scc0 .Ldn_ring_1
	s_sub_u32 s20, s20, 0x28000
.Ldn_ring_1:
	s_add_u32 m0, s20, 0x0
	s_nop 0
	global_load_lds_dwordx4 v2, s[16:17]
	s_add_u32 m0, s20, 0x1000
	s_nop 0
	global_load_lds_dwordx4 v3, s[16:17]
	s_add_u32 m0, s20, 0x2000
	s_nop 0
	global_load_lds_dwordx4 v4, s[16:17]
	s_add_u32 m0, s20, 0x3000
	s_nop 0
	global_load_lds_dwordx4 v5, s[16:17]
	s_add_u32 m0, s20, 0x4000
	s_nop 0
	global_load_lds_dwordx4 v2, s[18:19]
	s_add_u32 m0, s20, 0x5000
	s_nop 0
	global_load_lds_dwordx4 v3, s[18:19]
	s_add_u32 m0, s20, 0x6000
	s_nop 0
	global_load_lds_dwordx4 v4, s[18:19]
	s_add_u32 m0, s20, 0x7000
	s_nop 0
	global_load_lds_dwordx4 v5, s[18:19]
	s_add_u32 m0, s20, 0x8000
	s_nop 0
	global_load_lds_dwordx4 v6, s[18:19]
	s_add_u32 m0, s20, 0x9000
	s_nop 0
	global_load_lds_dwordx4 v7, s[18:19]
	s_add_u32 s16, s16, 0x80
	s_addc_u32 s17, s17, 0
	s_add_u32 s18, s18, 0x80
	s_addc_u32 s19, s19, 0
	s_add_u32 s20, s20, 0xa000
	s_cmp_ge_u32 s20, 0x28000
	s_cbranch_scc0 .Ldn_ring_2
	s_sub_u32 s20, s20, 0x28000

.Ldn_ring_3:
	s_add_u32 m0, s20, 0x0
	s_nop 0
	global_load_lds_dwordx4 v2, s[16:17]
	s_add_u32 m0, s20, 0x1000
	s_nop 0
	global_load_lds_dwordx4 v3, s[16:17]
	s_add_u32 m0, s20, 0x2000
	s_nop 0
	global_load_lds_dwordx4 v4, s[16:17]
	s_add_u32 m0, s20, 0x3000
	s_nop 0
	global_load_lds_dwordx4 v5, s[16:17]
	s_add_u32 m0, s20, 0x4000
	s_nop 0
	global_load_lds_dwordx4 v2, s[18:19]
	v_mov_b32_e32 v64, 0
	v_mov_b32_e32 v65, 0
	v_mov_b32_e32 v66, 0
	v_mov_b32_e32 v67, 0
	v_mov_b32_e32 v68, 0
	v_mov_b32_e32 v69, 0
	v_mov_b32_e32 v70, 0
	v_mov_b32_e32 v71, 0
	v_mov_b32_e32 v72, 0
	v_mov_b32_e32 v73, 0
	v_mov_b32_e32 v74, 0
	v_mov_b32_e32 v75, 0
	v_mov_b32_e32 v76, 0
	v_mov_b32_e32 v77, 0
	v_mov_b32_e32 v78, 0
	v_mov_b32_e32 v79, 0
	v_mov_b32_e32 v80, 0
	v_mov_b32_e32 v81, 0
	v_mov_b32_e32 v82, 0
	v_mov_b32_e32 v83, 0
	v_mov_b32_e32 v84, 0
	v_mov_b32_e32 v85, 0
	v_mov_b32_e32 v86, 0
	v_mov_b32_e32 v87, 0
	v_mov_b32_e32 v88, 0
	v_mov_b32_e32 v89, 0
	v_mov_b32_e32 v90, 0
	v_mov_b32_e32 v91, 0
	v_mov_b32_e32 v92, 0
	v_mov_b32_e32 v93, 0
	v_mov_b32_e32 v94, 0
	v_mov_b32_e32 v95, 0
	v_mov_b32_e32 v96, 0
	v_mov_b32_e32 v97, 0
	v_mov_b32_e32 v98, 0
	v_mov_b32_e32 v99, 0
	v_mov_b32_e32 v100, 0
	v_mov_b32_e32 v101, 0
	v_mov_b32_e32 v102, 0
	v_mov_b32_e32 v103, 0
	v_mov_b32_e32 v104, 0
	v_mov_b32_e32 v105, 0
	v_mov_b32_e32 v106, 0
	v_mov_b32_e32 v107, 0
	v_mov_b32_e32 v108, 0
	v_mov_b32_e32 v109, 0
	v_mov_b32_e32 v110, 0
	v_mov_b32_e32 v111, 0
	v_mov_b32_e32 v112, 0
	v_mov_b32_e32 v113, 0
	v_mov_b32_e32 v114, 0
	v_mov_b32_e32 v115, 0
	v_mov_b32_e32 v116, 0
	v_mov_b32_e32 v117, 0
	v_mov_b32_e32 v118, 0
	v_mov_b32_e32 v119, 0
	v_mov_b32_e32 v120, 0
	v_mov_b32_e32 v121, 0
	v_mov_b32_e32 v122, 0
	v_mov_b32_e32 v123, 0
	v_mov_b32_e32 v124, 0
	v_mov_b32_e32 v125, 0
	v_mov_b32_e32 v126, 0
	v_mov_b32_e32 v127, 0
	v_mov_b32_e32 v128, 0
	v_mov_b32_e32 v129, 0
	v_mov_b32_e32 v130, 0
	v_mov_b32_e32 v131, 0
	v_mov_b32_e32 v132, 0
	v_mov_b32_e32 v133, 0
	v_mov_b32_e32 v134, 0
	v_mov_b32_e32 v135, 0
	v_mov_b32_e32 v136, 0
	v_mov_b32_e32 v137, 0
	v_mov_b32_e32 v138, 0
	v_mov_b32_e32 v139, 0
	v_mov_b32_e32 v140, 0
	v_mov_b32_e32 v141, 0
	v_mov_b32_e32 v142, 0
	v_mov_b32_e32 v143, 0
	v_mov_b32_e32 v144, 0
	v_mov_b32_e32 v145, 0
	v_mov_b32_e32 v146, 0
	v_mov_b32_e32 v147, 0
	v_mov_b32_e32 v148, 0
	v_mov_b32_e32 v149, 0
	v_mov_b32_e32 v150, 0
	v_mov_b32_e32 v151, 0
	v_mov_b32_e32 v152, 0
	v_mov_b32_e32 v153, 0
	v_mov_b32_e32 v154, 0
	v_mov_b32_e32 v155, 0
	v_mov_b32_e32 v156, 0
	v_mov_b32_e32 v157, 0
	v_mov_b32_e32 v158, 0
	v_mov_b32_e32 v159, 0
	s_waitcnt vmcnt(25)
	s_barrier
	v_add_u32_e32 v10, s21, v8
	v_add_u32_e32 v12, s21, v9
	v_xor_b32_e32 v11, 64, v10
	v_xor_b32_e32 v13, 64, v12
	s_add_u32 s21, s21, 0xa000
	s_cmp_ge_u32 s21, 0x28000
	s_cbranch_scc0 .Ldn_ring_4
	s_sub_u32 s21, s21, 0x28000

.Ldn_loop:
	s_waitcnt lgkmcnt(10)
	v_mfma_f32_16x16x32_bf16 v[64:67], v[176:179], v[160:163], v[64:67]
	v_mfma_f32_16x16x32_bf16 v[68:71], v[176:179], v[164:167], v[68:71]
	s_add_u32 m0, s20, 0x5000
	v_mfma_f32_16x16x32_bf16 v[72:75], v[176:179], v[168:171], v[72:75]
	v_mfma_f32_16x16x32_bf16 v[76:79], v[176:179], v[172:175], v[76:79]
	global_load_lds_dwordx4 v3, s[18:19]
	v_mfma_f32_16x16x32_bf16 v[80:83], v[180:183], v[160:163], v[80:83]
	v_mfma_f32_16x16x32_bf16 v[84:87], v[180:183], v[164:167], v[84:87]
	s_add_u32 m0, s20, 0x6000
	v_mfma_f32_16x16x32_bf16 v[88:91], v[180:183], v[168:171], v[88:91]
	v_mfma_f32_16x16x32_bf16 v[92:95], v[180:183], v[172:175], v[92:95]
	global_load_lds_dwordx4 v4, s[18:19]
	v_mfma_f32_16x16x32_bf16 v[96:99], v[184:187], v[160:163], v[96:99]
	v_mfma_f32_16x16x32_bf16 v[100:103], v[184:187], v[164:167], v[100:103]
	s_add_u32 m0, s20, 0x7000
	v_mfma_f32_16x16x32_bf16 v[104:107], v[184:187], v[168:171], v[104:107]
	v_mfma_f32_16x16x32_bf16 v[108:111], v[184:187], v[172:175], v[108:111]
	global_load_lds_dwordx4 v5, s[18:19]
	v_mfma_f32_16x16x32_bf16 v[112:115], v[188:191], v[160:163], v[112:115]
	v_mfma_f32_16x16x32_bf16 v[116:119], v[188:191], v[164:167], v[116:119]
	s_add_u32 m0, s20, 0x8000
	v_mfma_f32_16x16x32_bf16 v[120:123], v[188:191], v[168:171], v[120:123]
	v_mfma_f32_16x16x32_bf16 v[124:127], v[188:191], v[172:175], v[124:127]
	global_load_lds_dwordx4 v6, s[18:19]
	v_mfma_f32_16x16x32_bf16 v[128:131], v[192:195], v[160:163], v[128:131]
	v_mfma_f32_16x16x32_bf16 v[132:135], v[192:195], v[164:167], v[132:135]
	s_add_u32 m0, s20, 0x9000
	v_mfma_f32_16x16x32_bf16 v[136:139], v[192:195], v[168:171], v[136:139]
	v_mfma_f32_16x16x32_bf16 v[140:143], v[192:195], v[172:175], v[140:143]
	global_load_lds_dwordx4 v7, s[18:19]
	v_mfma_f32_16x16x32_bf16 v[144:147], v[196:199], v[160:163], v[144:147]
	v_mfma_f32_16x16x32_bf16 v[148:151], v[196:199], v[164:167], v[148:151]
	v_mfma_f32_16x16x32_bf16 v[152:155], v[196:199], v[168:171], v[152:155]
	v_mfma_f32_16x16x32_bf16 v[156:159], v[196:199], v[172:175], v[156:159]
	s_add_u32 s16, s16, 0x80
	s_addc_u32 s17, s17, 0
	s_add_u32 s18, s18, 0x80
	s_addc_u32 s19, s19, 0
	s_add_u32 s20, s20, 0xa000
	s_cmp_ge_u32 s20, 0x28000
	s_cbranch_scc0 .Ldn_ring_5
	s_sub_u32 s20, s20, 0x28000
.Ldn_ring_5:
	s_waitcnt vmcnt(20) lgkmcnt(0)
	s_barrier
	v_add_u32_e32 v10, s21, v8
	v_add_u32_e32 v12, s21, v9
	v_xor_b32_e32 v11, 64, v10
	v_xor_b32_e32 v13, 64, v12
	s_add_u32 s21, s21, 0xa000
	s_cmp_ge_u32 s21, 0x28000
	s_cbranch_scc0 .Ldn_ring_6
	s_sub_u32 s21, s21, 0x28000
.Ldn_ring_6:
	v_mfma_f32_16x16x32_bf16 v[64:67], v[216:219], v[200:203], v[64:67]
	ds_read_b128 v[160:163], v10 offset:0
	v_mfma_f32_16x16x32_bf16 v[68:71], v[216:219], v[204:207], v[68:71]
	s_add_u32 m0, s20, 0x0
	v_mfma_f32_16x16x32_bf16 v[72:75], v[216:219], v[208:211], v[72:75]
	ds_read_b128 v[164:167], v10 offset:2048
	v_mfma_f32_16x16x32_bf16 v[76:79], v[216:219], v[212:215], v[76:79]
	global_load_lds_dwordx4 v2, s[16:17]
	v_mfma_f32_16x16x32_bf16 v[80:83], v[220:223], v[200:203], v[80:83]
	ds_read_b128 v[168:171], v10 offset:4096
	v_mfma_f32_16x16x32_bf16 v[84:87], v[220:223], v[204:207], v[84:87]
	s_add_u32 m0, s20, 0x1000
	v_mfma_f32_16x16x32_bf16 v[88:91], v[220:223], v[208:211], v[88:91]
	ds_read_b128 v[172:175], v10 offset:6144
	v_mfma_f32_16x16x32_bf16 v[92:95], v[220:223], v[212:215], v[92:95]
	global_load_lds_dwordx4 v3, s[16:17]
	v_mfma_f32_16x16x32_bf16 v[96:99], v[224:227], v[200:203], v[96:99]
	ds_read_b128 v[176:179], v12 offset:0
	v_mfma_f32_16x16x32_bf16 v[100:103], v[224:227], v[204:207], v[100:103]
	s_add_u32 m0, s20, 0x2000
	v_mfma_f32_16x16x32_bf16 v[104:107], v[224:227], v[208:211], v[104:107]
	ds_read_b128 v[180:183], v12 offset:2048
	v_mfma_f32_16x16x32_bf16 v[108:111], v[224:227], v[212:215], v[108:111]
	global_load_lds_dwordx4 v4, s[16:17]
	v_mfma_f32_16x16x32_bf16 v[112:115], v[228:231], v[200:203], v[112:115]
	ds_read_b128 v[184:187], v12 offset:4096
	v_mfma_f32_16x16x32_bf16 v[116:119], v[228:231], v[204:207], v[116:119]
	s_add_u32 m0, s20, 0x3000
	v_mfma_f32_16x16x32_bf16 v[120:123], v[228:231], v[208:211], v[120:123]
	ds_read_b128 v[188:191], v12 offset:6144
	v_mfma_f32_16x16x32_bf16 v[124:127], v[228:231], v[212:215], v[124:127]
	global_load_lds_dwordx4 v5, s[16:17]
	v_mfma_f32_16x16x32_bf16 v[128:131], v[232:235], v[200:203], v[128:131]
	ds_read_b128 v[192:195], v12 offset:8192
	v_mfma_f32_16x16x32_bf16 v[132:135], v[232:235], v[204:207], v[132:135]
	s_add_u32 m0, s20, 0x4000
	v_mfma_f32_16x16x32_bf16 v[136:139], v[232:235], v[208:211], v[136:139]
	ds_read_b128 v[196:199], v12 offset:10240
	v_mfma_f32_16x16x32_bf16 v[140:143], v[232:235], v[212:215], v[140:143]
	global_load_lds_dwordx4 v2, s[18:19]
	v_mfma_f32_16x16x32_bf16 v[144:147], v[236:239], v[200:203], v[144:147]
	v_mfma_f32_16x16x32_bf16 v[148:151], v[236:239], v[204:207], v[148:151]
	v_mfma_f32_16x16x32_bf16 v[152:155], v[236:239], v[208:211], v[152:155]
	v_mfma_f32_16x16x32_bf16 v[156:159], v[236:239], v[212:215], v[156:159]
	ds_read_b128 v[200:203], v11 offset:0
	ds_read_b128 v[204:207], v11 offset:2048
	ds_read_b128 v[208:211], v11 offset:4096
	ds_read_b128 v[212:215], v11 offset:6144
	ds_read_b128 v[216:219], v13 offset:0
	ds_read_b128 v[220:223], v13 offset:2048
	ds_read_b128 v[224:227], v13 offset:4096
	ds_read_b128 v[228:231], v13 offset:6144
	ds_read_b128 v[232:235], v13 offset:8192
	ds_read_b128 v[236:239], v13 offset:10240
	s_add_u32 s15, s15, 1
	s_cmp_lt_u32 s15, 44
	s_cbranch_scc1 .Ldn_loop
	s_waitcnt lgkmcnt(10)
	v_mfma_f32_16x16x32_bf16 v[64:67], v[176:179], v[160:163], v[64:67]
	v_mfma_f32_16x16x32_bf16 v[68:71], v[176:179], v[164:167], v[68:71]
	s_add_u32 m0, s20, 0x5000
	v_mfma_f32_16x16x32_bf16 v[72:75], v[176:179], v[168:171], v[72:75]
	v_mfma_f32_16x16x32_bf16 v[76:79], v[176:179], v[172:175], v[76:79]
	global_load_lds_dwordx4 v3, s[18:19]
	v_mfma_f32_16x16x32_bf16 v[80:83], v[180:183], v[160:163], v[80:83]
	v_mfma_f32_16x16x32_bf16 v[84:87], v[180:183], v[164:167], v[84:87]
	s_add_u32 m0, s20, 0x6000
	v_mfma_f32_16x16x32_bf16 v[88:91], v[180:183], v[168:171], v[88:91]
	v_mfma_f32_16x16x32_bf16 v[92:95], v[180:183], v[172:175], v[92:95]
	global_load_lds_dwordx4 v4, s[18:19]
	v_mfma_f32_16x16x32_bf16 v[96:99], v[184:187], v[160:163], v[96:99]
	v_mfma_f32_16x16x32_bf16 v[100:103], v[184:187], v[164:167], v[100:103]
	s_add_u32 m0, s20, 0x7000
	v_mfma_f32_16x16x32_bf16 v[104:107], v[184:187], v[168:171], v[104:107]
	v_mfma_f32_16x16x32_bf16 v[108:111], v[184:187], v[172:175], v[108:111]
	global_load_lds_dwordx4 v5, s[18:19]
	v_mfma_f32_16x16x32_bf16 v[112:115], v[188:191], v[160:163], v[112:115]
	v_mfma_f32_16x16x32_bf16 v[116:119], v[188:191], v[164:167], v[116:119]
	s_add_u32 m0, s20, 0x8000
	v_mfma_f32_16x16x32_bf16 v[120:123], v[188:191], v[168:171], v[120:123]
	v_mfma_f32_16x16x32_bf16 v[124:127], v[188:191], v[172:175], v[124:127]
	global_load_lds_dwordx4 v6, s[18:19]
	v_mfma_f32_16x16x32_bf16 v[128:131], v[192:195], v[160:163], v[128:131]
	v_mfma_f32_16x16x32_bf16 v[132:135], v[192:195], v[164:167], v[132:135]
	s_add_u32 m0, s20, 0x9000
	v_mfma_f32_16x16x32_bf16 v[136:139], v[192:195], v[168:171], v[136:139]
	v_mfma_f32_16x16x32_bf16 v[140:143], v[192:195], v[172:175], v[140:143]
	global_load_lds_dwordx4 v7, s[18:19]
	v_mfma_f32_16x16x32_bf16 v[144:147], v[196:199], v[160:163], v[144:147]
	v_mfma_f32_16x16x32_bf16 v[148:151], v[196:199], v[164:167], v[148:151]
	v_mfma_f32_16x16x32_bf16 v[152:155], v[196:199], v[168:171], v[152:155]
	v_mfma_f32_16x16x32_bf16 v[156:159], v[196:199], v[172:175], v[156:159]
	s_add_u32 s16, s16, 0x80
	s_addc_u32 s17, s17, 0
	s_add_u32 s18, s18, 0x80
	s_addc_u32 s19, s19, 0
	s_add_u32 s20, s20, 0xa000
	s_cmp_ge_u32 s20, 0x28000
	s_cbranch_scc0 .Ldn_ring_7
	s_sub_u32 s20, s20, 0x28000

.Ldn_ring_8:
	v_mfma_f32_16x16x32_bf16 v[64:67], v[216:219], v[200:203], v[64:67]
	ds_read_b128 v[160:163], v10 offset:0
	v_mfma_f32_16x16x32_bf16 v[68:71], v[216:219], v[204:207], v[68:71]
	ds_read_b128 v[164:167], v10 offset:2048
	v_mfma_f32_16x16x32_bf16 v[72:75], v[216:219], v[208:211], v[72:75]
	ds_read_b128 v[168:171], v10 offset:4096
	v_mfma_f32_16x16x32_bf16 v[76:79], v[216:219], v[212:215], v[76:79]
	ds_read_b128 v[172:175], v10 offset:6144
	v_mfma_f32_16x16x32_bf16 v[80:83], v[220:223], v[200:203], v[80:83]
	ds_read_b128 v[176:179], v12 offset:0
	v_mfma_f32_16x16x32_bf16 v[84:87], v[220:223], v[204:207], v[84:87]
	ds_read_b128 v[180:183], v12 offset:2048
	v_mfma_f32_16x16x32_bf16 v[88:91], v[220:223], v[208:211], v[88:91]
	ds_read_b128 v[184:187], v12 offset:4096
	v_mfma_f32_16x16x32_bf16 v[92:95], v[220:223], v[212:215], v[92:95]
	ds_read_b128 v[188:191], v12 offset:6144
	v_mfma_f32_16x16x32_bf16 v[96:99], v[224:227], v[200:203], v[96:99]
	ds_read_b128 v[192:195], v12 offset:8192
	v_mfma_f32_16x16x32_bf16 v[100:103], v[224:227], v[204:207], v[100:103]
	ds_read_b128 v[196:199], v12 offset:10240
	v_mfma_f32_16x16x32_bf16 v[104:107], v[224:227], v[208:211], v[104:107]
	v_mfma_f32_16x16x32_bf16 v[108:111], v[224:227], v[212:215], v[108:111]
	v_mfma_f32_16x16x32_bf16 v[112:115], v[228:231], v[200:203], v[112:115]
	v_mfma_f32_16x16x32_bf16 v[116:119], v[228:231], v[204:207], v[116:119]
	v_mfma_f32_16x16x32_bf16 v[120:123], v[228:231], v[208:211], v[120:123]
	v_mfma_f32_16x16x32_bf16 v[124:127], v[228:231], v[212:215], v[124:127]
	v_mfma_f32_16x16x32_bf16 v[128:131], v[232:235], v[200:203], v[128:131]
	v_mfma_f32_16x16x32_bf16 v[132:135], v[232:235], v[204:207], v[132:135]
	v_mfma_f32_16x16x32_bf16 v[136:139], v[232:235], v[208:211], v[136:139]
	v_mfma_f32_16x16x32_bf16 v[140:143], v[232:235], v[212:215], v[140:143]
	v_mfma_f32_16x16x32_bf16 v[144:147], v[236:239], v[200:203], v[144:147]
	v_mfma_f32_16x16x32_bf16 v[148:151], v[236:239], v[204:207], v[148:151]
	v_mfma_f32_16x16x32_bf16 v[152:155], v[236:239], v[208:211], v[152:155]
	v_mfma_f32_16x16x32_bf16 v[156:159], v[236:239], v[212:215], v[156:159]
	ds_read_b128 v[200:203], v11 offset:0
	ds_read_b128 v[204:207], v11 offset:2048
	ds_read_b128 v[208:211], v11 offset:4096
	ds_read_b128 v[212:215], v11 offset:6144
	ds_read_b128 v[216:219], v13 offset:0
	ds_read_b128 v[220:223], v13 offset:2048
	ds_read_b128 v[224:227], v13 offset:4096
	ds_read_b128 v[228:231], v13 offset:6144
	ds_read_b128 v[232:235], v13 offset:8192
	ds_read_b128 v[236:239], v13 offset:10240
	s_waitcnt lgkmcnt(10)
	v_mfma_f32_16x16x32_bf16 v[64:67], v[176:179], v[160:163], v[64:67]
	v_mfma_f32_16x16x32_bf16 v[68:71], v[176:179], v[164:167], v[68:71]
	v_mfma_f32_16x16x32_bf16 v[72:75], v[176:179], v[168:171], v[72:75]
	v_mfma_f32_16x16x32_bf16 v[76:79], v[176:179], v[172:175], v[76:79]
	v_mfma_f32_16x16x32_bf16 v[80:83], v[180:183], v[160:163], v[80:83]
	v_mfma_f32_16x16x32_bf16 v[84:87], v[180:183], v[164:167], v[84:87]
	v_mfma_f32_16x16x32_bf16 v[88:91], v[180:183], v[168:171], v[88:91]
	v_mfma_f32_16x16x32_bf16 v[92:95], v[180:183], v[172:175], v[92:95]
	v_mfma_f32_16x16x32_bf16 v[96:99], v[184:187], v[160:163], v[96:99]
	v_mfma_f32_16x16x32_bf16 v[100:103], v[184:187], v[164:167], v[100:103]
	v_mfma_f32_16x16x32_bf16 v[104:107], v[184:187], v[168:171], v[104:107]
	v_mfma_f32_16x16x32_bf16 v[108:111], v[184:187], v[172:175], v[108:111]
	v_mfma_f32_16x16x32_bf16 v[112:115], v[188:191], v[160:163], v[112:115]
	v_mfma_f32_16x16x32_bf16 v[116:119], v[188:191], v[164:167], v[116:119]
	v_mfma_f32_16x16x32_bf16 v[120:123], v[188:191], v[168:171], v[120:123]
	v_mfma_f32_16x16x32_bf16 v[124:127], v[188:191], v[172:175], v[124:127]
	v_mfma_f32_16x16x32_bf16 v[128:131], v[192:195], v[160:163], v[128:131]
	v_mfma_f32_16x16x32_bf16 v[132:135], v[192:195], v[164:167], v[132:135]
	v_mfma_f32_16x16x32_bf16 v[136:139], v[192:195], v[168:171], v[136:139]
	v_mfma_f32_16x16x32_bf16 v[140:143], v[192:195], v[172:175], v[140:143]
	v_mfma_f32_16x16x32_bf16 v[144:147], v[196:199], v[160:163], v[144:147]
	v_mfma_f32_16x16x32_bf16 v[148:151], v[196:199], v[164:167], v[148:151]
	v_mfma_f32_16x16x32_bf16 v[152:155], v[196:199], v[168:171], v[152:155]
	v_mfma_f32_16x16x32_bf16 v[156:159], v[196:199], v[172:175], v[156:159]
	s_waitcnt vmcnt(10) lgkmcnt(0)
	s_barrier
	v_add_u32_e32 v10, s21, v8
	v_add_u32_e32 v12, s21, v9
	v_xor_b32_e32 v11, 64, v10
	v_xor_b32_e32 v13, 64, v12
	s_add_u32 s21, s21, 0xa000
	s_cmp_ge_u32 s21, 0x28000
	s_cbranch_scc0 .Ldn_ring_9
	s_sub_u32 s21, s21, 0x28000
.Ldn_ring_9:
	v_mfma_f32_16x16x32_bf16 v[64:67], v[216:219], v[200:203], v[64:67]
	ds_read_b128 v[160:163], v10 offset:0
	v_mfma_f32_16x16x32_bf16 v[68:71], v[216:219], v[204:207], v[68:71]
	ds_read_b128 v[164:167], v10 offset:2048
	v_mfma_f32_16x16x32_bf16 v[72:75], v[216:219], v[208:211], v[72:75]
	ds_read_b128 v[168:171], v10 offset:4096
	v_mfma_f32_16x16x32_bf16 v[76:79], v[216:219], v[212:215], v[76:79]
	ds_read_b128 v[172:175], v10 offset:6144
	v_mfma_f32_16x16x32_bf16 v[80:83], v[220:223], v[200:203], v[80:83]
	ds_read_b128 v[176:179], v12 offset:0
	v_mfma_f32_16x16x32_bf16 v[84:87], v[220:223], v[204:207], v[84:87]
	ds_read_b128 v[180:183], v12 offset:2048
	v_mfma_f32_16x16x32_bf16 v[88:91], v[220:223], v[208:211], v[88:91]
	ds_read_b128 v[184:187], v12 offset:4096
	v_mfma_f32_16x16x32_bf16 v[92:95], v[220:223], v[212:215], v[92:95]
	ds_read_b128 v[188:191], v12 offset:6144
	v_mfma_f32_16x16x32_bf16 v[96:99], v[224:227], v[200:203], v[96:99]
	ds_read_b128 v[192:195], v12 offset:8192
	v_mfma_f32_16x16x32_bf16 v[100:103], v[224:227], v[204:207], v[100:103]
	ds_read_b128 v[196:199], v12 offset:10240
	v_mfma_f32_16x16x32_bf16 v[104:107], v[224:227], v[208:211], v[104:107]
	v_mfma_f32_16x16x32_bf16 v[108:111], v[224:227], v[212:215], v[108:111]
	v_mfma_f32_16x16x32_bf16 v[112:115], v[228:231], v[200:203], v[112:115]
	v_mfma_f32_16x16x32_bf16 v[116:119], v[228:231], v[204:207], v[116:119]
	v_mfma_f32_16x16x32_bf16 v[120:123], v[228:231], v[208:211], v[120:123]
	v_mfma_f32_16x16x32_bf16 v[124:127], v[228:231], v[212:215], v[124:127]
	v_mfma_f32_16x16x32_bf16 v[128:131], v[232:235], v[200:203], v[128:131]
	v_mfma_f32_16x16x32_bf16 v[132:135], v[232:235], v[204:207], v[132:135]
	v_mfma_f32_16x16x32_bf16 v[136:139], v[232:235], v[208:211], v[136:139]
	v_mfma_f32_16x16x32_bf16 v[140:143], v[232:235], v[212:215], v[140:143]
	v_mfma_f32_16x16x32_bf16 v[144:147], v[236:239], v[200:203], v[144:147]
	v_mfma_f32_16x16x32_bf16 v[148:151], v[236:239], v[204:207], v[148:151]
	v_mfma_f32_16x16x32_bf16 v[152:155], v[236:239], v[208:211], v[152:155]
	v_mfma_f32_16x16x32_bf16 v[156:159], v[236:239], v[212:215], v[156:159]
	ds_read_b128 v[200:203], v11 offset:0
	ds_read_b128 v[204:207], v11 offset:2048
	ds_read_b128 v[208:211], v11 offset:4096
	ds_read_b128 v[212:215], v11 offset:6144
	ds_read_b128 v[216:219], v13 offset:0
	ds_read_b128 v[220:223], v13 offset:2048
	ds_read_b128 v[224:227], v13 offset:4096
	ds_read_b128 v[228:231], v13 offset:6144
	ds_read_b128 v[232:235], v13 offset:8192
	ds_read_b128 v[236:239], v13 offset:10240
	s_waitcnt lgkmcnt(10)
	v_mfma_f32_16x16x32_bf16 v[64:67], v[176:179], v[160:163], v[64:67]
	v_mfma_f32_16x16x32_bf16 v[68:71], v[176:179], v[164:167], v[68:71]
	v_mfma_f32_16x16x32_bf16 v[72:75], v[176:179], v[168:171], v[72:75]
	v_mfma_f32_16x16x32_bf16 v[76:79], v[176:179], v[172:175], v[76:79]
	v_mfma_f32_16x16x32_bf16 v[80:83], v[180:183], v[160:163], v[80:83]
	v_mfma_f32_16x16x32_bf16 v[84:87], v[180:183], v[164:167], v[84:87]
	v_mfma_f32_16x16x32_bf16 v[88:91], v[180:183], v[168:171], v[88:91]
	v_mfma_f32_16x16x32_bf16 v[92:95], v[180:183], v[172:175], v[92:95]
	v_mfma_f32_16x16x32_bf16 v[96:99], v[184:187], v[160:163], v[96:99]
	v_mfma_f32_16x16x32_bf16 v[100:103], v[184:187], v[164:167], v[100:103]
	v_mfma_f32_16x16x32_bf16 v[104:107], v[184:187], v[168:171], v[104:107]
	v_mfma_f32_16x16x32_bf16 v[108:111], v[184:187], v[172:175], v[108:111]
	v_mfma_f32_16x16x32_bf16 v[112:115], v[188:191], v[160:163], v[112:115]
	v_mfma_f32_16x16x32_bf16 v[116:119], v[188:191], v[164:167], v[116:119]
	v_mfma_f32_16x16x32_bf16 v[120:123], v[188:191], v[168:171], v[120:123]
	v_mfma_f32_16x16x32_bf16 v[124:127], v[188:191], v[172:175], v[124:127]
	v_mfma_f32_16x16x32_bf16 v[128:131], v[192:195], v[160:163], v[128:131]
	v_mfma_f32_16x16x32_bf16 v[132:135], v[192:195], v[164:167], v[132:135]
	v_mfma_f32_16x16x32_bf16 v[136:139], v[192:195], v[168:171], v[136:139]
	v_mfma_f32_16x16x32_bf16 v[140:143], v[192:195], v[172:175], v[140:143]
	v_mfma_f32_16x16x32_bf16 v[144:147], v[196:199], v[160:163], v[144:147]
	v_mfma_f32_16x16x32_bf16 v[148:151], v[196:199], v[164:167], v[148:151]
	v_mfma_f32_16x16x32_bf16 v[152:155], v[196:199], v[168:171], v[152:155]
	v_mfma_f32_16x16x32_bf16 v[156:159], v[196:199], v[172:175], v[156:159]
	s_waitcnt vmcnt(0) lgkmcnt(0)
	s_barrier
	v_add_u32_e32 v10, s21, v8
	v_add_u32_e32 v12, s21, v9
	v_xor_b32_e32 v11, 64, v10
	v_xor_b32_e32 v13, 64, v12
	s_add_u32 s21, s21, 0xa000
	s_cmp_ge_u32 s21, 0x28000
	s_cbranch_scc0 .Ldn_ring_10
	s_sub_u32 s21, s21, 0x28000
.Ldn_ring_10:
	v_mfma_f32_16x16x32_bf16 v[64:67], v[216:219], v[200:203], v[64:67]
	ds_read_b128 v[160:163], v10 offset:0
	v_mfma_f32_16x16x32_bf16 v[68:71], v[216:219], v[204:207], v[68:71]
	global_load_dwordx4 v[16:19], v56, s[8:9] offset:0
	v_mfma_f32_16x16x32_bf16 v[72:75], v[216:219], v[208:211], v[72:75]
	ds_read_b128 v[164:167], v10 offset:2048
	v_mfma_f32_16x16x32_bf16 v[76:79], v[216:219], v[212:215], v[76:79]
	global_load_dwordx4 v[20:23], v57, s[8:9] offset:0
	v_mfma_f32_16x16x32_bf16 v[80:83], v[220:223], v[200:203], v[80:83]
	ds_read_b128 v[168:171], v10 offset:4096
	v_mfma_f32_16x16x32_bf16 v[84:87], v[220:223], v[204:207], v[84:87]
	global_load_dwordx4 v[24:27], v58, s[8:9] offset:0
	v_mfma_f32_16x16x32_bf16 v[88:91], v[220:223], v[208:211], v[88:91]
	ds_read_b128 v[172:175], v10 offset:6144
	v_mfma_f32_16x16x32_bf16 v[92:95], v[220:223], v[212:215], v[92:95]
	global_load_dwordx4 v[28:31], v59, s[8:9] offset:0
	v_mfma_f32_16x16x32_bf16 v[96:99], v[224:227], v[200:203], v[96:99]
	ds_read_b128 v[176:179], v12 offset:0
	v_mfma_f32_16x16x32_bf16 v[100:103], v[224:227], v[204:207], v[100:103]
	global_load_dwordx4 v[32:35], v56, s[8:9] offset:64
	v_mfma_f32_16x16x32_bf16 v[104:107], v[224:227], v[208:211], v[104:107]
	ds_read_b128 v[180:183], v12 offset:2048
	v_mfma_f32_16x16x32_bf16 v[108:111], v[224:227], v[212:215], v[108:111]
	global_load_dwordx4 v[36:39], v57, s[8:9] offset:64
	v_mfma_f32_16x16x32_bf16 v[112:115], v[228:231], v[200:203], v[112:115]
	ds_read_b128 v[184:187], v12 offset:4096
	v_mfma_f32_16x16x32_bf16 v[116:119], v[228:231], v[204:207], v[116:119]
	global_load_dwordx4 v[40:43], v58, s[8:9] offset:64
	v_mfma_f32_16x16x32_bf16 v[120:123], v[228:231], v[208:211], v[120:123]
	ds_read_b128 v[188:191], v12 offset:6144
	v_mfma_f32_16x16x32_bf16 v[124:127], v[228:231], v[212:215], v[124:127]
	global_load_dwordx4 v[44:47], v59, s[8:9] offset:64
	v_mfma_f32_16x16x32_bf16 v[128:131], v[232:235], v[200:203], v[128:131]
	ds_read_b128 v[192:195], v12 offset:8192
	v_mfma_f32_16x16x32_bf16 v[132:135], v[232:235], v[204:207], v[132:135]
	global_load_dwordx4 v[48:51], v56, s[8:9] offset:128
	v_mfma_f32_16x16x32_bf16 v[136:139], v[232:235], v[208:211], v[136:139]
	ds_read_b128 v[196:199], v12 offset:10240
	v_mfma_f32_16x16x32_bf16 v[140:143], v[232:235], v[212:215], v[140:143]
	global_load_dwordx4 v[52:55], v57, s[8:9] offset:128
	v_mfma_f32_16x16x32_bf16 v[144:147], v[236:239], v[200:203], v[144:147]
	global_load_dwordx4 v[240:243], v58, s[8:9] offset:128
	v_mfma_f32_16x16x32_bf16 v[148:151], v[236:239], v[204:207], v[148:151]
	global_load_dwordx4 v[244:247], v59, s[8:9] offset:128
	v_mfma_f32_16x16x32_bf16 v[152:155], v[236:239], v[208:211], v[152:155]
	global_load_dwordx4 v[248:251], v56, s[8:9] offset:192
	v_mfma_f32_16x16x32_bf16 v[156:159], v[236:239], v[212:215], v[156:159]
	global_load_dwordx4 v[252:255], v57, s[8:9] offset:192
	ds_read_b128 v[200:203], v11 offset:0
	ds_read_b128 v[204:207], v11 offset:2048
	ds_read_b128 v[208:211], v11 offset:4096
	ds_read_b128 v[212:215], v11 offset:6144
	ds_read_b128 v[216:219], v13 offset:0
	ds_read_b128 v[220:223], v13 offset:2048
	ds_read_b128 v[224:227], v13 offset:4096
	ds_read_b128 v[228:231], v13 offset:6144
	ds_read_b128 v[232:235], v13 offset:8192
	ds_read_b128 v[236:239], v13 offset:10240
	s_waitcnt lgkmcnt(10)
	v_mfma_f32_16x16x32_bf16 v[64:67], v[176:179], v[160:163], v[64:67]
	v_mfma_f32_16x16x32_bf16 v[68:71], v[176:179], v[164:167], v[68:71]
	v_mfma_f32_16x16x32_bf16 v[72:75], v[176:179], v[168:171], v[72:75]
	v_mfma_f32_16x16x32_bf16 v[76:79], v[176:179], v[172:175], v[76:79]
	v_mfma_f32_16x16x32_bf16 v[80:83], v[180:183], v[160:163], v[80:83]
	v_mfma_f32_16x16x32_bf16 v[84:87], v[180:183], v[164:167], v[84:87]
	v_mfma_f32_16x16x32_bf16 v[88:91], v[180:183], v[168:171], v[88:91]
	v_mfma_f32_16x16x32_bf16 v[92:95], v[180:183], v[172:175], v[92:95]
	v_mfma_f32_16x16x32_bf16 v[96:99], v[184:187], v[160:163], v[96:99]
	v_mfma_f32_16x16x32_bf16 v[100:103], v[184:187], v[164:167], v[100:103]
	v_mfma_f32_16x16x32_bf16 v[104:107], v[184:187], v[168:171], v[104:107]
	v_mfma_f32_16x16x32_bf16 v[108:111], v[184:187], v[172:175], v[108:111]
	v_mfma_f32_16x16x32_bf16 v[112:115], v[188:191], v[160:163], v[112:115]
	v_mfma_f32_16x16x32_bf16 v[116:119], v[188:191], v[164:167], v[116:119]
	v_mfma_f32_16x16x32_bf16 v[120:123], v[188:191], v[168:171], v[120:123]
	v_mfma_f32_16x16x32_bf16 v[124:127], v[188:191], v[172:175], v[124:127]
	v_mfma_f32_16x16x32_bf16 v[128:131], v[192:195], v[160:163], v[128:131]
	v_mfma_f32_16x16x32_bf16 v[132:135], v[192:195], v[164:167], v[132:135]
	v_mfma_f32_16x16x32_bf16 v[136:139], v[192:195], v[168:171], v[136:139]
	v_mfma_f32_16x16x32_bf16 v[140:143], v[192:195], v[172:175], v[140:143]
	v_mfma_f32_16x16x32_bf16 v[144:147], v[196:199], v[160:163], v[144:147]
	v_mfma_f32_16x16x32_bf16 v[148:151], v[196:199], v[164:167], v[148:151]
	v_mfma_f32_16x16x32_bf16 v[152:155], v[196:199], v[168:171], v[152:155]
	v_mfma_f32_16x16x32_bf16 v[156:159], v[196:199], v[172:175], v[156:159]
	s_waitcnt lgkmcnt(0)
	v_mfma_f32_16x16x32_bf16 v[64:67], v[216:219], v[200:203], v[64:67]
	v_mfma_f32_16x16x32_bf16 v[68:71], v[216:219], v[204:207], v[68:71]
	global_load_dwordx4 v[160:163], v58, s[8:9] offset:192
	v_mfma_f32_16x16x32_bf16 v[72:75], v[216:219], v[208:211], v[72:75]
	v_mfma_f32_16x16x32_bf16 v[76:79], v[216:219], v[212:215], v[76:79]
	global_load_dwordx4 v[164:167], v59, s[8:9] offset:192
	v_mfma_f32_16x16x32_bf16 v[80:83], v[220:223], v[200:203], v[80:83]
	v_mfma_f32_16x16x32_bf16 v[84:87], v[220:223], v[204:207], v[84:87]
	global_load_dwordx4 v[168:171], v56, s[8:9] offset:256
	v_mfma_f32_16x16x32_bf16 v[88:91], v[220:223], v[208:211], v[88:91]
	v_mfma_f32_16x16x32_bf16 v[92:95], v[220:223], v[212:215], v[92:95]
	global_load_dwordx4 v[172:175], v57, s[8:9] offset:256
	v_mfma_f32_16x16x32_bf16 v[96:99], v[224:227], v[200:203], v[96:99]
	v_mfma_f32_16x16x32_bf16 v[100:103], v[224:227], v[204:207], v[100:103]
	global_load_dwordx4 v[176:179], v58, s[8:9] offset:256
	v_mfma_f32_16x16x32_bf16 v[104:107], v[224:227], v[208:211], v[104:107]
	v_mfma_f32_16x16x32_bf16 v[108:111], v[224:227], v[212:215], v[108:111]
	global_load_dwordx4 v[180:183], v59, s[8:9] offset:256
	v_mfma_f32_16x16x32_bf16 v[112:115], v[228:231], v[200:203], v[112:115]
	v_mfma_f32_16x16x32_bf16 v[116:119], v[228:231], v[204:207], v[116:119]
	global_load_dwordx4 v[184:187], v56, s[8:9] offset:320
	v_mfma_f32_16x16x32_bf16 v[120:123], v[228:231], v[208:211], v[120:123]
	v_mfma_f32_16x16x32_bf16 v[124:127], v[228:231], v[212:215], v[124:127]
	global_load_dwordx4 v[188:191], v57, s[8:9] offset:320
	v_mfma_f32_16x16x32_bf16 v[128:131], v[232:235], v[200:203], v[128:131]
	v_mfma_f32_16x16x32_bf16 v[132:135], v[232:235], v[204:207], v[132:135]
	global_load_dwordx4 v[192:195], v58, s[8:9] offset:320
	v_mfma_f32_16x16x32_bf16 v[136:139], v[232:235], v[208:211], v[136:139]
	v_mfma_f32_16x16x32_bf16 v[140:143], v[232:235], v[212:215], v[140:143]
	global_load_dwordx4 v[196:199], v59, s[8:9] offset:320
	v_mfma_f32_16x16x32_bf16 v[144:147], v[236:239], v[200:203], v[144:147]
	v_mfma_f32_16x16x32_bf16 v[148:151], v[236:239], v[204:207], v[148:151]
	v_mfma_f32_16x16x32_bf16 v[152:155], v[236:239], v[208:211], v[152:155]
	v_mfma_f32_16x16x32_bf16 v[156:159], v[236:239], v[212:215], v[156:159]
	s_waitcnt vmcnt(23)
	v_pk_add_f32 v[64:65], v[64:65], v[16:17]
	v_pk_add_f32 v[66:67], v[66:67], v[18:19]
	global_store_dwordx4 v56, v[64:67], s[10:11] offset:0
	s_waitcnt vmcnt(23)
	v_pk_add_f32 v[68:69], v[68:69], v[20:21]
	v_pk_add_f32 v[70:71], v[70:71], v[22:23]
	global_store_dwordx4 v57, v[68:71], s[10:11] offset:0
	s_waitcnt vmcnt(23)
	v_pk_add_f32 v[72:73], v[72:73], v[24:25]
	v_pk_add_f32 v[74:75], v[74:75], v[26:27]
	global_store_dwordx4 v58, v[72:75], s[10:11] offset:0
	s_waitcnt vmcnt(23)
	v_pk_add_f32 v[76:77], v[76:77], v[28:29]
	v_pk_add_f32 v[78:79], v[78:79], v[30:31]
	global_store_dwordx4 v59, v[76:79], s[10:11] offset:0
	s_waitcnt vmcnt(23)
	v_pk_add_f32 v[80:81], v[80:81], v[32:33]
	v_pk_add_f32 v[82:83], v[82:83], v[34:35]
	global_store_dwordx4 v56, v[80:83], s[10:11] offset:64
	s_waitcnt vmcnt(23)
	v_pk_add_f32 v[84:85], v[84:85], v[36:37]
	v_pk_add_f32 v[86:87], v[86:87], v[38:39]
	global_store_dwordx4 v57, v[84:87], s[10:11] offset:64
	s_waitcnt vmcnt(23)
	v_pk_add_f32 v[88:89], v[88:89], v[40:41]
	v_pk_add_f32 v[90:91], v[90:91], v[42:43]
	global_store_dwordx4 v58, v[88:91], s[10:11] offset:64
	s_waitcnt vmcnt(23)
	v_pk_add_f32 v[92:93], v[92:93], v[44:45]
	v_pk_add_f32 v[94:95], v[94:95], v[46:47]
	global_store_dwordx4 v59, v[92:95], s[10:11] offset:64
	s_waitcnt vmcnt(23)
	v_pk_add_f32 v[96:97], v[96:97], v[48:49]
	v_pk_add_f32 v[98:99], v[98:99], v[50:51]
	global_store_dwordx4 v56, v[96:99], s[10:11] offset:128
	s_waitcnt vmcnt(23)
	v_pk_add_f32 v[100:101], v[100:101], v[52:53]
	v_pk_add_f32 v[102:103], v[102:103], v[54:55]
	global_store_dwordx4 v57, v[100:103], s[10:11] offset:128
	s_waitcnt vmcnt(23)
	v_pk_add_f32 v[104:105], v[104:105], v[240:241]
	v_pk_add_f32 v[106:107], v[106:107], v[242:243]
	global_store_dwordx4 v58, v[104:107], s[10:11] offset:128
	s_waitcnt vmcnt(23)
	v_pk_add_f32 v[108:109], v[108:109], v[244:245]
	v_pk_add_f32 v[110:111], v[110:111], v[246:247]
	global_store_dwordx4 v59, v[108:111], s[10:11] offset:128
	s_waitcnt vmcnt(23)
	v_pk_add_f32 v[112:113], v[112:113], v[248:249]
	v_pk_add_f32 v[114:115], v[114:115], v[250:251]
	global_store_dwordx4 v56, v[112:115], s[10:11] offset:192
	s_waitcnt vmcnt(23)
	v_pk_add_f32 v[116:117], v[116:117], v[252:253]
	v_pk_add_f32 v[118:119], v[118:119], v[254:255]
	global_store_dwordx4 v57, v[116:119], s[10:11] offset:192
	s_waitcnt vmcnt(23)
	v_pk_add_f32 v[120:121], v[120:121], v[160:161]
	v_pk_add_f32 v[122:123], v[122:123], v[162:163]
	global_store_dwordx4 v58, v[120:123], s[10:11] offset:192
	s_waitcnt vmcnt(23)
	v_pk_add_f32 v[124:125], v[124:125], v[164:165]
	v_pk_add_f32 v[126:127], v[126:127], v[166:167]
	global_store_dwordx4 v59, v[124:127], s[10:11] offset:192
	s_waitcnt vmcnt(23)
	v_pk_add_f32 v[128:129], v[128:129], v[168:169]
	v_pk_add_f32 v[130:131], v[130:131], v[170:171]
	global_store_dwordx4 v56, v[128:131], s[10:11] offset:256
	s_waitcnt vmcnt(23)
	v_pk_add_f32 v[132:133], v[132:133], v[172:173]
	v_pk_add_f32 v[134:135], v[134:135], v[174:175]
	global_store_dwordx4 v57, v[132:135], s[10:11] offset:256
	s_waitcnt vmcnt(23)
	v_pk_add_f32 v[136:137], v[136:137], v[176:177]
	v_pk_add_f32 v[138:139], v[138:139], v[178:179]
	global_store_dwordx4 v58, v[136:139], s[10:11] offset:256
	s_waitcnt vmcnt(23)
	v_pk_add_f32 v[140:141], v[140:141], v[180:181]
	v_pk_add_f32 v[142:143], v[142:143], v[182:183]
	global_store_dwordx4 v59, v[140:143], s[10:11] offset:256
	s_waitcnt vmcnt(23)
	v_pk_add_f32 v[144:145], v[144:145], v[184:185]
	v_pk_add_f32 v[146:147], v[146:147], v[186:187]
	global_store_dwordx4 v56, v[144:147], s[10:11] offset:320
	s_waitcnt vmcnt(23)
	v_pk_add_f32 v[148:149], v[148:149], v[188:189]
	v_pk_add_f32 v[150:151], v[150:151], v[190:191]
	global_store_dwordx4 v57, v[148:151], s[10:11] offset:320
	s_waitcnt vmcnt(23)
	v_pk_add_f32 v[152:153], v[152:153], v[192:193]
	v_pk_add_f32 v[154:155], v[154:155], v[194:195]
	global_store_dwordx4 v58, v[152:155], s[10:11] offset:320
	s_waitcnt vmcnt(23)
	v_pk_add_f32 v[156:157], v[156:157], v[196:197]
	v_pk_add_f32 v[158:159], v[158:159], v[198:199]
	global_store_dwordx4 v59, v[156:159], s[10:11] offset:320

	.amdhsa_kernel _Z7gemm128ILi3ELi96EEv8GemmArgs
		.amdhsa_group_segment_fixed_size 98304
		.amdhsa_private_segment_fixed_size 0
		.amdhsa_kernarg_size 80
		.amdhsa_user_sgpr_count 2
		.amdhsa_user_sgpr_dispatch_ptr 0
		.amdhsa_user_sgpr_queue_ptr 0
		.amdhsa_user_sgpr_kernarg_segment_ptr 1
		.amdhsa_user_sgpr_dispatch_id 0
		.amdhsa_user_sgpr_kernarg_preload_length 0
		.amdhsa_user_sgpr_kernarg_preload_offset 0
		.amdhsa_user_sgpr_private_segment_size 0
		.amdhsa_uses_dynamic_stack 0
		.amdhsa_enable_private_segment 0
		.amdhsa_system_sgpr_workgroup_id_x 1
		.amdhsa_system_sgpr_workgroup_id_y 0
		.amdhsa_system_sgpr_workgroup_id_z 0
		.amdhsa_system_sgpr_workgroup_info 0
		.amdhsa_system_vgpr_workitem_id 0
		.amdhsa_next_free_vgpr 256
		.amdhsa_next_free_sgpr 24
		.amdhsa_accum_offset 256
		.amdhsa_reserve_vcc 1
		.amdhsa_float_round_mode_32 0
		.amdhsa_float_round_mode_16_64 0
		.amdhsa_float_denorm_mode_32 3
		.amdhsa_float_denorm_mode_16_64 3
		.amdhsa_dx10_clamp 1
		.amdhsa_ieee_mode 1
		.amdhsa_fp16_overflow 0
		.amdhsa_tg_split 0
		.amdhsa_exception_fp_ieee_invalid_op 0
		.amdhsa_exception_fp_denorm_src 0
		.amdhsa_exception_fp_ieee_div_zero 0
		.amdhsa_exception_fp_ieee_overflow 0
		.amdhsa_exception_fp_ieee_underflow 0
		.amdhsa_exception_fp_ieee_inexact 0
		.amdhsa_exception_int_div_zero 0
	.end_amdhsa_kernel

amdhsa.kernels:
  - .agpr_count:     0
    .args:
      - .offset:         0
        .size:           136
        .value_kind:     by_value
      - .offset:         136
        .size:           4
        .value_kind:     hidden_block_count_x
      - .offset:         140
        .size:           4
        .value_kind:     hidden_block_count_y
      - .offset:         144
        .size:           4
        .value_kind:     hidden_block_count_z
      - .offset:         148
        .size:           2
        .value_kind:     hidden_group_size_x
      - .offset:         150
        .size:           2
        .value_kind:     hidden_group_size_y
      - .offset:         152
        .size:           2
        .value_kind:     hidden_group_size_z
      - .offset:         154
        .size:           2
        .value_kind:     hidden_remainder_x
      - .offset:         156
        .size:           2
        .value_kind:     hidden_remainder_y
      - .offset:         158
        .size:           2
        .value_kind:     hidden_remainder_z
      - .offset:         176
        .size:           8
        .value_kind:     hidden_global_offset_x
      - .offset:         184
        .size:           8
        .value_kind:     hidden_global_offset_y
      - .offset:         192
        .size:           8
        .value_kind:     hidden_global_offset_z
      - .offset:         200
        .size:           2
        .value_kind:     hidden_grid_dims
    .group_segment_fixed_size: 16640
    .kernarg_segment_align: 8
    .kernarg_segment_size: 392
    .language:       OpenCL C
    .language_version:
      - 2
      - 0
    .max_flat_workgroup_size: 256
    .name:           _Z11prep_kernel8PrepArgs
    .private_segment_fixed_size: 0
    .sgpr_count:     26
    .sgpr_spill_count: 0
    .symbol:         _Z11prep_kernel8PrepArgs.kd
    .uniform_work_group_size: 1
    .uses_dynamic_stack: false
    .vgpr_count:     46
    .vgpr_spill_count: 0
    .wavefront_size: 64
  - .agpr_count:     0
    .args:
      - .offset:         0
        .size:           216
        .value_kind:     by_value
    .group_segment_fixed_size: 0
    .kernarg_segment_align: 8
    .kernarg_segment_size: 216
    .language:       OpenCL C
    .language_version:
      - 2
      - 0
    .max_flat_workgroup_size: 512
    .name:           _Z11attn_kernel8AttnArgs
    .private_segment_fixed_size: 0
    .sgpr_count:     82
    .sgpr_spill_count: 0
    .symbol:         _Z11attn_kernel8AttnArgs.kd
    .uniform_work_group_size: 1
    .uses_dynamic_stack: false
    .vgpr_count:     220
    .vgpr_spill_count: 0
    .wavefront_size: 64
  - .agpr_count:     0
    .args:
      - .offset:         0
        .size:           80
        .value_kind:     by_value
    .group_segment_fixed_size: 0
    .kernarg_segment_align: 8
    .kernarg_segment_size: 80
    .language:       OpenCL C
    .language_version:
      - 2
      - 0
    .max_flat_workgroup_size: 256
    .name:           _Z7gemm128ILi1ELi96EEv8GemmArgs
    .private_segment_fixed_size: 0
    .sgpr_count:     26
    .sgpr_spill_count: 0
    .symbol:         _Z7gemm128ILi1ELi96EEv8GemmArgs.kd
    .uniform_work_group_size: 1
    .uses_dynamic_stack: false
    .vgpr_count:     141
    .vgpr_spill_count: 0
    .wavefront_size: 64
  - .agpr_count:     0
    .args:
      - .offset:         0
        .size:           80
        .value_kind:     by_value
    .group_segment_fixed_size: 0
    .kernarg_segment_align: 8
    .kernarg_segment_size: 80
    .language:       OpenCL C
    .language_version:
      - 2
      - 0
    .max_flat_workgroup_size: 256
    .name:           _Z7gemm128ILi2ELi128EEv8GemmArgs
    .private_segment_fixed_size: 0
    .sgpr_count:     22
    .sgpr_spill_count: 0
    .symbol:         _Z7gemm128ILi2ELi128EEv8GemmArgs.kd
    .uniform_work_group_size: 1
    .uses_dynamic_stack: false
    .vgpr_count:     166
    .vgpr_spill_count: 0
    .wavefront_size: 64
  - .agpr_count:     0
    .args:
      - .offset:         0
        .size:           80
        .value_kind:     by_value
    .group_segment_fixed_size: 98304
    .kernarg_segment_align: 8
    .kernarg_segment_size: 80
    .language:       OpenCL C
    .language_version:
      - 2
      - 0
    .max_flat_workgroup_size: 256
    .name:           _Z7gemm128ILi3ELi96EEv8GemmArgs
    .private_segment_fixed_size: 0
    .sgpr_count:     30
    .sgpr_spill_count: 0
    .symbol:         _Z7gemm128ILi3ELi96EEv8GemmArgs.kd
    .uniform_work_group_size: 1
    .uses_dynamic_stack: false
    .vgpr_count:     256
    .vgpr_spill_count: 0
    .wavefront_size: 64
  - .agpr_count:     0
    .args:
      - .offset:         0
        .size:           32
        .value_kind:     by_value
      - .offset:         32
        .size:           56
        .value_kind:     by_value
    .group_segment_fixed_size: 0
    .kernarg_segment_align: 8
    .kernarg_segment_size: 88
    .language:       OpenCL C
    .language_version:
      - 2
      - 0
    .max_flat_workgroup_size: 512
    .name:           _Z8gemm_bigIN3pg86EpiQKVEEvNS0_4GemmET_
    .private_segment_fixed_size: 0
    .sgpr_count:     58
    .sgpr_spill_count: 0
    .symbol:         _Z8gemm_bigIN3pg86EpiQKVEEvNS0_4GemmET_.kd
    .uniform_work_group_size: 1
    .uses_dynamic_stack: false
    .vgpr_count:     228
    .vgpr_spill_count: 0
    .wavefront_size: 64
  - .agpr_count:     0
    .args:
      - .offset:         0
        .size:           32
        .value_kind:     by_value
      - .offset:         32
        .size:           32
        .value_kind:     by_value
    .group_segment_fixed_size: 0
    .kernarg_segment_align: 8
    .kernarg_segment_size: 64
    .language:       OpenCL C
    .language_version:
      - 2
      - 0
    .max_flat_workgroup_size: 512
    .name:           _Z8gemm_bigIN3pg85EpiUPEEvNS0_4GemmET_
    .private_segment_fixed_size: 0
    .sgpr_count:     50
    .sgpr_spill_count: 0
    .symbol:         _Z8gemm_bigIN3pg85EpiUPEEvNS0_4GemmET_.kd
    .uniform_work_group_size: 1
    .uses_dynamic_stack: false
    .vgpr_count:     226
    .vgpr_spill_count: 0
    .wavefront_size: 64
